# baseline (speedup 1.0000x reference)
.LBB1_13:
.LBB1_14:
	ds_read_b32 v4, v4 offset:34816
	s_waitcnt vmcnt(0) lgkmcnt(1)
	v_lshrrev_b32_e32 v7, 5, v8
	v_lshlrev_b32_e64 v9, v8, 1
	v_cmp_eq_u32_e32 vcc, v3, v7
	v_lshl_add_u32 v10, 2, v8, -1
	v_readfirstlane_b32 s3, v7
	s_add_i32 s43, s3, 1
	s_cmp_lt_u32 s3, 15
	s_cselect_b32 s41, s43, 15
	v_readlane_b32 s42, v6, s41
	s_cselect_b32 s42, s42, 0
	v_cndmask_b32_e32 v9, 0, v9, vcc
	v_cndmask_b32_e32 v10, 0, v10, vcc
	v_cmp_ge_u32_e32 vcc, v3, v7
	v_or_b32_e32 v16, v6, v9
	s_movk_i32 s15, 0x410
	v_cndmask_b32_e32 v10, -1, v10, vcc
	s_waitcnt lgkmcnt(0)
	v_and_b32_e32 v4, v4, v10
	v_cmp_le_u32_e32 vcc, v3, v7
	v_and_b32_e32 v2, 63, v0
	s_nop 0
	v_cndmask_b32_e32 v4, -1, v4, vcc
	v_cmp_ne_u32_e32 vcc, s43, v3
	s_nop 1
	v_cndmask_b32_e32 v4, 0, v4, vcc
	v_bitop3_b32 v4, v4, v6, v9 bitop3:0xe0
	v_bitop3_b32 v6, v6, v10, v9 bitop3:0x32
	v_bcnt_u32_b32 v12, v4, 0
	v_readlane_b32 s3, v6, s3
	v_bcnt_u32_b32 v6, v16, 0
	v_lshlrev_b32_e32 v13, 16, v6
	v_or_b32_e32 v6, v12, v13
	v_mov_b32_e32 v9, 0
	v_mov_b64_e32 v[10:11], s[10:11]
	v_mov_b32_dpp v17, v6 row_shr:1 row_mask:0xf bank_mask:0xf bound_ctrl:1
	v_add_u32_e32 v6, v6, v17
	v_cmp_gt_u32_e32 vcc, 16, v2
	s_nop 0
	v_mov_b32_dpp v18, v6 row_shr:2 row_mask:0xf bank_mask:0xf bound_ctrl:1
	v_add_u32_e32 v6, v6, v18
	s_nop 1
	v_mov_b32_dpp v19, v6 row_shr:4 row_mask:0xf bank_mask:0xf bound_ctrl:1
	v_add_u32_e32 v6, v6, v19
	s_nop 1
	v_mov_b32_dpp v20, v6 row_shr:8 row_mask:0xf bank_mask:0xf bound_ctrl:1
	v_add_u32_e32 v21, v6, v20
	v_lshl_add_u64 v[6:7], s[4:5], 0, v[8:9]
	v_mad_u64_u32 v[10:11], s[4:5], v6, s15, v[10:11]
	v_cmp_ne_u32_e64 s[4:5], 0, v4
	v_readlane_b32 s18, v21, 15
	v_mad_u32_u24 v11, v7, s15, v11
	s_and_b64 s[10:11], vcc, s[4:5]
	s_and_saveexec_b64 s[4:5], s[10:11]
	s_cbranch_execz .LBB1_21
	v_mul_hi_u32_u24_e32 v23, 48, v8
	v_mul_u32_u24_e32 v22, 48, v8
	v_mov_b32_e32 v8, 0x6000
	v_mad_u64_u32 v[22:23], s[10:11], s14, v8, v[22:23]
	v_add_u32_e32 v8, v17, v18
	v_add3_u32 v8, v8, v19, v20
	v_add3_u32 v8, v8, v12, v13
	v_sub_u32_sdwa v21, v21, v12 dst_sel:DWORD dst_unused:UNUSED_PAD src0_sel:WORD_0 src1_sel:DWORD
	v_sub_u32_sdwa v12, v8, v12 dst_sel:DWORD dst_unused:UNUSED_PAD src0_sel:WORD_0 src1_sel:DWORD
	v_ashrrev_i32_e32 v13, 31, v12
	v_lshl_add_u64 v[12:13], v[12:13], 1, v[22:23]
	v_lshlrev_b32_e32 v3, 5, v3
	v_lshl_add_u64 v[12:13], s[8:9], 0, v[12:13]
	s_mov_b64 s[10:11], 0
	v_mov_b32_e32 v8, v21
	s_branch .LBB1_17

.LBB1_25:
	s_or_b64 exec, exec, s[4:5]
	v_cmp_eq_u32_e32 vcc, 0, v2
	s_and_saveexec_b64 s[4:5], vcc
	s_cbranch_execz .LBB1_27
	v_lshl_add_u64 v[6:7], v[6:7], 4, s[12:13]
	v_mov_b32_e32 v2, s10
	v_mov_b32_e32 v3, s3
	v_lshl_or_b32 v2, v5, 16, v2
	v_mov_b32_e32 v5, s42
	global_store_dwordx4 v[6:7], v[2:5], off
